# removed the grid barrier between the weight-conversion prologue and the layer-0 residual phase (no data dependence between them)
# baseline (speedup 1.0000x reference)
.LBB0_107:
	s_or_b64 exec, exec, s[4:5]
.LBB0_173:
	s_cmp_gt_i32 s34, 1
	s_cselect_b64 s[2:3], -1, 0
	s_cmp_lt_i32 s35, 2
	s_cselect_b64 s[4:5], -1, 0
	s_or_b64 s[2:3], s[2:3], s[4:5]
	s_and_b64 vcc, exec, s[2:3]
	s_cbranch_vccnz .LBB0_249
	s_mov_b32 s2, 24
	s_lshl_b32 s2, s2, 3
	s_add_i32 s4, 0, 0x201c0
	s_add_i32 s2, s4, s2
	v_mov_b32_e32 v0, s2
	s_mov_b32 s3, 0
	ds_read_b32 v1, v0
	ds_read_b32 v0, v0 offset:4
	s_lshl_b32 s2, s3, 3
	s_add_i32 s2, s4, s2
	v_mov_b32_e32 v2, s2
	ds_read_b32 v3, v2
	s_waitcnt lgkmcnt(2)
	v_readfirstlane_b32 s8, v1
	ds_read_b32 v1, v2 offset:4
	s_load_dword s24, s[0:1], 0xd0
	s_add_u32 s6, s0, 0xd0
	s_addc_u32 s7, s1, 0
	s_waitcnt lgkmcnt(0)
	v_readfirstlane_b32 s9, v0
	v_readfirstlane_b32 s4, v3
	s_mov_b32 s2, s24
	s_and_b32 s2, s2, 7
	s_cmp_lg_u32 s2, 0
	v_readfirstlane_b32 s5, v1
	s_cbranch_scc0 .LBB0_194
	s_mov_b32 s12, s10
	s_cbranch_execnz .LBB0_177
